# stack of the individually-neutral edits on v48: N2(0) drain rebalance + NA half-tile trimming + MLA H0 K prefetch + barrier release-before-invalidate + unscaled fp8 MFMA form
# speedup vs baseline: 1.0096x; 1.0014x over previous
.LBB0_563:
	s_or_b64 exec, exec, s[2:3]
	v_mul_f32_e32 v0, v108, v0
	v_mul_f32_e32 v1, v108, v1
	v_mul_f32_e32 v27, v108, v27
	v_mul_f32_e32 v0, v0, v114
	v_mul_f32_e32 v1, v1, v113
	v_mul_f32_e32 v27, v27, v135
	v_med3_f32 v0, v0, s69, v203
	v_med3_f32 v1, v1, s69, v203
	v_mov_b32_e32 v135, v187
	v_cvt_pk_fp8_f32 v135, v0, v1
	v_mul_f32_e32 v2, v108, v2
	v_mul_f32_e32 v3, v108, v3
	v_mul_f32_e32 v2, v2, v112
	v_mul_f32_e32 v3, v3, v111
	v_med3_f32 v0, v2, s69, v203
	v_med3_f32 v1, v3, s69, v203
	v_mul_f32_e32 v26, v108, v26
	v_cvt_pk_fp8_f32 v135, v0, v1 op_sel:[0,0,1]
	v_max_f32_e32 v0, v106, v106
	v_max_f32_e32 v1, v107, v107
	v_mul_f32_e32 v26, v26, v136
	v_med3_f32 v0, v0, s69, v203
	v_med3_f32 v1, v1, s69, v203
	v_mov_b32_e32 v136, v187
	v_cvt_pk_fp8_f32 v136, v0, v1
	v_max_f32_e32 v2, v102, v102
	v_max_f32_e32 v1, v103, v103
	v_med3_f32 v0, v2, s69, v203
	v_med3_f32 v1, v1, s69, v203
	v_mul_f32_e32 v25, v108, v25
	v_cvt_pk_fp8_f32 v136, v0, v1 op_sel:[0,0,1]
	v_max_f32_e32 v0, v100, v100
	v_max_f32_e32 v1, v101, v101
	v_mul_f32_e32 v25, v25, v137
	v_med3_f32 v0, v0, s69, v203
	v_med3_f32 v1, v1, s69, v203
	v_mov_b32_e32 v137, v187
	v_cvt_pk_fp8_f32 v137, v0, v1
	v_max_f32_e32 v2, v98, v98
	v_max_f32_e32 v1, v99, v99
	v_med3_f32 v0, v2, s69, v203
	v_med3_f32 v1, v1, s69, v203
	v_mul_f32_e32 v24, v108, v24
	v_cvt_pk_fp8_f32 v137, v0, v1 op_sel:[0,0,1]
	v_max_f32_e32 v0, v96, v96
	v_max_f32_e32 v1, v97, v97
	v_mul_f32_e32 v24, v24, v138
	v_med3_f32 v0, v0, s69, v203
	v_med3_f32 v1, v1, s69, v203
	v_mov_b32_e32 v138, v187
	v_cvt_pk_fp8_f32 v138, v0, v1
	v_max_f32_e32 v2, v94, v94
	v_max_f32_e32 v1, v95, v95
	v_med3_f32 v0, v2, s69, v203
	v_med3_f32 v1, v1, s69, v203
	v_mul_f32_e32 v31, v108, v31
	v_cvt_pk_fp8_f32 v138, v0, v1 op_sel:[0,0,1]
	v_max_f32_e32 v0, v92, v92
	v_max_f32_e32 v1, v93, v93
	v_mul_f32_e32 v31, v31, v139
	v_med3_f32 v0, v0, s69, v203
	v_med3_f32 v1, v1, s69, v203
	v_mov_b32_e32 v139, v187
	v_cvt_pk_fp8_f32 v139, v0, v1
	v_max_f32_e32 v2, v90, v90
	v_max_f32_e32 v1, v91, v91
	v_med3_f32 v0, v2, s69, v203
	v_med3_f32 v1, v1, s69, v203
	v_mul_f32_e32 v30, v108, v30
	v_cvt_pk_fp8_f32 v139, v0, v1 op_sel:[0,0,1]
	v_max_f32_e32 v0, v88, v88
	v_max_f32_e32 v1, v89, v89
	v_mul_f32_e32 v30, v30, v140
	v_med3_f32 v0, v0, s69, v203
	v_med3_f32 v1, v1, s69, v203
	v_mov_b32_e32 v140, v187
	v_cvt_pk_fp8_f32 v140, v0, v1
	v_max_f32_e32 v2, v86, v86
	v_max_f32_e32 v1, v87, v87
	v_med3_f32 v0, v2, s69, v203
	v_med3_f32 v1, v1, s69, v203
	v_mul_f32_e32 v29, v108, v29
	v_cvt_pk_fp8_f32 v140, v0, v1 op_sel:[0,0,1]
	v_max_f32_e32 v0, v84, v84
	v_max_f32_e32 v1, v85, v85
	v_mul_f32_e32 v29, v29, v141
	v_med3_f32 v0, v0, s69, v203
	v_med3_f32 v1, v1, s69, v203
	v_mov_b32_e32 v141, v187
	v_cvt_pk_fp8_f32 v141, v0, v1
	v_max_f32_e32 v2, v82, v82
	v_max_f32_e32 v1, v83, v83
	v_med3_f32 v0, v2, s69, v203
	v_med3_f32 v1, v1, s69, v203
	v_mul_f32_e32 v28, v108, v28
	v_cvt_pk_fp8_f32 v141, v0, v1 op_sel:[0,0,1]
	v_max_f32_e32 v0, v80, v80
	v_max_f32_e32 v1, v81, v81
	v_mul_f32_e32 v28, v28, v142
	v_med3_f32 v0, v0, s69, v203
	v_med3_f32 v1, v1, s69, v203
	v_mov_b32_e32 v142, v187
	v_cvt_pk_fp8_f32 v142, v0, v1
	v_mul_f32_e32 v4, v108, v4
	v_mul_f32_e32 v5, v108, v5
	v_mul_f32_e32 v60, v60, v108
	v_mul_f32_e32 v61, v61, v108
	v_mul_f32_e32 v56, v56, v108
	v_mul_f32_e32 v57, v57, v108
	v_mul_f32_e32 v52, v52, v108
	v_mul_f32_e32 v53, v108, v53
	v_mul_f32_e32 v48, v108, v48
	v_mul_f32_e32 v49, v108, v49
	v_mul_f32_e32 v44, v108, v44
	v_mul_f32_e32 v45, v108, v45
	v_mul_f32_e32 v40, v108, v40
	v_mul_f32_e32 v41, v108, v41
	v_mul_f32_e32 v36, v108, v36
	v_mul_f32_e32 v37, v108, v37
	v_mul_f32_e32 v32, v108, v32
	v_mul_f32_e32 v33, v108, v33
	v_mul_f32_e32 v20, v108, v20
	v_mul_f32_e32 v4, v4, v118
	v_mul_f32_e32 v5, v5, v117
	v_max_f32_e32 v2, v78, v78
	v_max_f32_e32 v1, v79, v79
	v_mul_f32_e32 v60, v60, v182
	v_mul_f32_e32 v61, v61, v181
	v_mul_f32_e32 v56, v56, v178
	v_mul_f32_e32 v57, v57, v177
	v_mul_f32_e32 v52, v52, v174
	v_mul_f32_e32 v53, v53, v173
	v_mul_f32_e32 v48, v48, v162
	v_mul_f32_e32 v49, v49, v161
	v_mul_f32_e32 v44, v44, v158
	v_mul_f32_e32 v45, v45, v157
	v_mul_f32_e32 v40, v40, v154
	v_mul_f32_e32 v41, v41, v153
	v_mul_f32_e32 v36, v36, v150
	v_mul_f32_e32 v37, v37, v149
	v_mul_f32_e32 v32, v32, v146
	v_mul_f32_e32 v33, v33, v145
	v_mul_f32_e32 v20, v20, v134
	v_mul_f32_e32 v19, v108, v19
	v_mul_f32_e32 v12, v108, v12
	v_mul_f32_e32 v13, v108, v13
	v_mul_f32_e32 v14, v108, v14
	v_mul_f32_e32 v15, v108, v15
	v_mul_f32_e32 v8, v108, v8
	v_mul_f32_e32 v9, v108, v9
	v_mul_f32_e32 v10, v108, v10
	v_med3_f32 v4, v4, s69, v203
	v_med3_f32 v5, v5, s69, v203
	v_mov_b32_e32 v134, v187
	v_med3_f32 v0, v2, s69, v203
	v_med3_f32 v1, v1, s69, v203
	v_mul_f32_e32 v35, v108, v35
	v_mul_f32_e32 v21, v108, v21
	v_mul_f32_e32 v19, v19, v127
	v_mul_f32_e32 v12, v12, v126
	v_mul_f32_e32 v13, v13, v125
	v_mul_f32_e32 v14, v14, v124
	v_mul_f32_e32 v15, v15, v123
	v_mul_f32_e32 v8, v8, v122
	v_mul_f32_e32 v9, v9, v121
	v_mul_f32_e32 v10, v10, v120
	v_med3_f32 v60, v60, s69, v203
	v_med3_f32 v61, v61, s69, v203
	v_mov_b32_e32 v120, v187
	v_med3_f32 v56, v56, s69, v203
	v_med3_f32 v57, v57, s69, v203
	v_mov_b32_e32 v121, v187
	v_med3_f32 v52, v52, s69, v203
	v_med3_f32 v53, v53, s69, v203
	v_mov_b32_e32 v122, v187
	v_med3_f32 v48, v48, s69, v203
	v_med3_f32 v49, v49, s69, v203
	v_mov_b32_e32 v123, v187
	v_med3_f32 v44, v44, s69, v203
	v_med3_f32 v45, v45, s69, v203
	v_mov_b32_e32 v124, v187
	v_med3_f32 v40, v40, s69, v203
	v_med3_f32 v41, v41, s69, v203
	v_mov_b32_e32 v125, v187
	v_med3_f32 v36, v36, s69, v203
	v_med3_f32 v37, v37, s69, v203
	v_mov_b32_e32 v126, v187
	v_med3_f32 v32, v32, s69, v203
	v_med3_f32 v33, v33, s69, v203
	v_mov_b32_e32 v127, v187
	v_cvt_pk_fp8_f32 v134, v4, v5
	v_cvt_pk_fp8_f32 v142, v0, v1 op_sel:[0,0,1]
	v_max_f32_e32 v0, v76, v76
	v_max_f32_e32 v1, v77, v77
	v_mul_f32_e32 v35, v35, v143
	v_mul_f32_e32 v21, v21, v133
	v_mul_f32_e32 v6, v108, v6
	v_mul_f32_e32 v7, v108, v7
	v_cvt_pk_fp8_f32 v120, v60, v61
	v_cvt_pk_fp8_f32 v121, v56, v57
	v_cvt_pk_fp8_f32 v122, v52, v53
	v_cvt_pk_fp8_f32 v123, v48, v49
	v_cvt_pk_fp8_f32 v124, v44, v45
	v_cvt_pk_fp8_f32 v125, v40, v41
	v_cvt_pk_fp8_f32 v126, v36, v37
	v_cvt_pk_fp8_f32 v127, v32, v33
	v_med3_f32 v8, v8, s69, v203
	v_med3_f32 v9, v9, s69, v203
	v_mov_b32_e32 v133, v187
	v_med3_f32 v0, v0, s69, v203
	v_med3_f32 v1, v1, s69, v203
	v_mov_b32_e32 v143, v187
	v_mul_f32_e32 v62, v62, v108
	v_mul_f32_e32 v63, v63, v108
	v_mul_f32_e32 v58, v58, v108
	v_mul_f32_e32 v59, v59, v108
	v_mul_f32_e32 v54, v108, v54
	v_mul_f32_e32 v55, v108, v55
	v_mul_f32_e32 v50, v108, v50
	v_mul_f32_e32 v51, v108, v51
	v_mul_f32_e32 v46, v108, v46
	v_mul_f32_e32 v47, v108, v47
	v_mul_f32_e32 v42, v108, v42
	v_mul_f32_e32 v43, v108, v43
	v_mul_f32_e32 v38, v108, v38
	v_mul_f32_e32 v39, v108, v39
	v_mul_f32_e32 v34, v108, v34
	v_mul_f32_e32 v16, v108, v16
	v_mul_f32_e32 v17, v108, v17
	v_mul_f32_e32 v6, v6, v116
	v_mul_f32_e32 v7, v7, v115
	v_cvt_pk_fp8_f32 v133, v8, v9
	v_cvt_pk_fp8_f32 v143, v0, v1
	v_mul_u32_u24_e32 v0, 0xd0, v186
	s_and_b32 s3, s17, 0x3fffffc0
	v_mul_f32_e32 v62, v62, v180
	v_mul_f32_e32 v63, v63, v179
	v_mul_f32_e32 v58, v58, v176
	v_mul_f32_e32 v59, v59, v175
	v_mul_f32_e32 v54, v54, v172
	v_mul_f32_e32 v55, v55, v163
	v_mul_f32_e32 v50, v50, v160
	v_mul_f32_e32 v51, v51, v159
	v_mul_f32_e32 v46, v46, v156
	v_mul_f32_e32 v47, v47, v155
	v_mul_f32_e32 v42, v42, v152
	v_mul_f32_e32 v43, v43, v151
	v_mul_f32_e32 v38, v38, v148
	v_mul_f32_e32 v39, v39, v147
	v_mul_f32_e32 v34, v34, v144
	v_mul_f32_e32 v23, v108, v23
	v_mul_f32_e32 v16, v16, v130
	v_mul_f32_e32 v17, v17, v129
	v_mul_f32_e32 v18, v108, v18
	v_mul_f32_e32 v11, v108, v11
	v_med3_f32 v6, v6, s69, v203
	v_med3_f32 v7, v7, s69, v203
	v_add3_u32 v216, 0, v0, v72
	s_lshl_b32 s3, s3, 2
	s_ashr_i32 s18, s18, 6
	v_mul_f32_e32 v23, v23, v131
	v_mul_f32_e32 v18, v18, v128
	v_mul_f32_e32 v11, v11, v119
	v_med3_f32 v62, v62, s69, v203
	v_med3_f32 v63, v63, s69, v203
	v_med3_f32 v56, v58, s69, v203
	v_med3_f32 v57, v59, s69, v203
	v_med3_f32 v54, v54, s69, v203
	v_med3_f32 v55, v55, s69, v203
	v_med3_f32 v48, v50, s69, v203
	v_med3_f32 v49, v51, s69, v203
	v_med3_f32 v46, v46, s69, v203
	v_med3_f32 v47, v47, s69, v203
	v_med3_f32 v40, v42, s69, v203
	v_med3_f32 v41, v43, s69, v203
	v_med3_f32 v38, v38, s69, v203
	v_med3_f32 v39, v39, s69, v203
	v_med3_f32 v32, v34, s69, v203
	v_med3_f32 v33, v35, s69, v203
	v_med3_f32 v28, v28, s69, v203
	v_med3_f32 v29, v29, s69, v203
	v_mov_b32_e32 v128, v187
	v_med3_f32 v24, v24, s69, v203
	v_med3_f32 v25, v25, s69, v203
	v_mov_b32_e32 v129, v187
	v_med3_f32 v20, v20, s69, v203
	v_med3_f32 v21, v21, s69, v203
	v_mov_b32_e32 v130, v187
	v_med3_f32 v16, v16, s69, v203
	v_med3_f32 v17, v17, s69, v203
	v_mov_b32_e32 v131, v187
	v_cvt_pk_fp8_f32 v134, v6, v7 op_sel:[0,0,1]
	ds_read_b128 v[0:3], v216
	ds_read_b128 v[4:7], v216 offset:16
	s_add_i32 s3, s3, 0
	s_ashr_i32 s19, s18, 31
	s_lshl_b32 s2, s74, 1
	v_cvt_pk_fp8_f32 v120, v62, v63 op_sel:[0,0,1]
	v_cvt_pk_fp8_f32 v121, v56, v57 op_sel:[0,0,1]
	v_cvt_pk_fp8_f32 v122, v54, v55 op_sel:[0,0,1]
	v_cvt_pk_fp8_f32 v123, v48, v49 op_sel:[0,0,1]
	v_cvt_pk_fp8_f32 v124, v46, v47 op_sel:[0,0,1]
	v_cvt_pk_fp8_f32 v125, v40, v41 op_sel:[0,0,1]
	v_cvt_pk_fp8_f32 v126, v38, v39 op_sel:[0,0,1]
	v_cvt_pk_fp8_f32 v127, v32, v33 op_sel:[0,0,1]
	v_cvt_pk_fp8_f32 v128, v28, v29
	v_cvt_pk_fp8_f32 v129, v24, v25
	v_cvt_pk_fp8_f32 v130, v20, v21
	v_cvt_pk_fp8_f32 v131, v16, v17
	v_med3_f32 v8, v10, s69, v203
	v_med3_f32 v9, v11, s69, v203
	s_add_i32 s79, s3, 0x18000
	s_lshl_b64 s[18:19], s[18:19], 16
	v_mul_f32_e32 v22, v108, v22
	v_cvt_pk_fp8_f32 v133, v8, v9 op_sel:[0,0,1]
	v_max_f32_e32 v8, v74, v74
	v_max_f32_e32 v9, v75, v75
	s_add_u32 s18, s44, s18
	v_mul_f32_e32 v22, v22, v132
	v_med3_f32 v8, v8, s69, v203
	v_med3_f32 v9, v9, s69, v203
	s_addc_u32 s19, s45, s19
	v_med3_f32 v30, v30, s69, v203
	v_med3_f32 v31, v31, s69, v203
	v_med3_f32 v24, v26, s69, v203
	v_med3_f32 v25, v27, s69, v203
	v_med3_f32 v22, v22, s69, v203
	v_med3_f32 v23, v23, s69, v203
	v_med3_f32 v16, v18, s69, v203
	v_med3_f32 v17, v19, s69, v203
	v_cvt_pk_fp8_f32 v143, v8, v9 op_sel:[0,0,1]
	v_lshl_add_u64 v[8:9], s[18:19], 0, v[104:105]
	v_cvt_pk_fp8_f32 v128, v30, v31 op_sel:[0,0,1]
	v_cvt_pk_fp8_f32 v129, v24, v25 op_sel:[0,0,1]
	v_cvt_pk_fp8_f32 v130, v22, v23 op_sel:[0,0,1]
	v_cvt_pk_fp8_f32 v131, v16, v17 op_sel:[0,0,1]
	s_waitcnt lgkmcnt(0)
	v_mfma_f32_32x32x64_f8f6f4 v[16:31], v[0:7], v[120:127], 0
	ds_read_b128 v[0:3], v216 offset:64
	ds_read_b128 v[4:7], v216 offset:80
	global_load_dwordx4 v[172:175], v[8:9], off
	v_med3_f32 v12, v12, s69, v203
	v_med3_f32 v13, v13, s69, v203
	v_mov_b32_e32 v132, v187
	v_cvt_pk_fp8_f32 v132, v12, v13
	v_med3_f32 v14, v14, s69, v203
	v_med3_f32 v15, v15, s69, v203
	s_mov_b32 s17, s16
	v_cvt_pk_fp8_f32 v132, v14, v15 op_sel:[0,0,1]
	s_mov_b32 s18, s16
	s_mov_b32 s19, s16
	s_mov_b32 s20, s16
	s_mov_b32 s21, s16
	s_mov_b32 s22, s16
	s_waitcnt lgkmcnt(0)
	v_mfma_f32_32x32x64_f8f6f4 v[16:31], v[0:7], v[128:135], v[16:31]
	v_sub_u32_e32 v0, v216, v73
	ds_read_b128 v[32:35], v0 offset:128
	ds_read_b128 v[36:39], v0 offset:160
	s_mov_b32 s23, s16
	s_mov_b32 s24, s16
	s_mov_b32 s25, s16
	s_mov_b32 s26, s16
	s_mov_b32 s27, s16
	s_mov_b32 s28, s16
	s_mov_b32 s29, s16
	s_mov_b32 s30, s16
	s_mov_b32 s31, s16
	v_mov_b64_e32 v[0:1], s[16:17]
	v_and_b32_e32 v64, 63, v110
	v_mov_b64_e32 v[14:15], s[30:31]
	v_mov_b64_e32 v[2:3], s[18:19]
	s_waitcnt lgkmcnt(0)
	v_mfma_f32_32x32x64_f8f6f4 v[16:31], v[32:39], v[136:143], v[16:31]
	v_mov_b64_e32 v[4:5], s[20:21]
	v_mov_b64_e32 v[6:7], s[22:23]
	v_mov_b64_e32 v[8:9], s[24:25]
	v_mov_b64_e32 v[10:11], s[26:27]
	v_mov_b64_e32 v[12:13], s[28:29]
	v_sub_u32_e32 v217, 0, v73
	v_mov_b32_e32 v112, 0x38383838
	v_mov_b64_e32 v[62:63], v[14:15]
	s_mov_b32 s78, 2
	v_lshl_add_u32 v209, v186, 2, s79
	v_mov_b32_e32 v113, v112
	v_mov_b32_e32 v114, v112
	v_mov_b32_e32 v115, v112
	v_mov_b32_e32 v116, v112
	s_nop 5
	v_max_f32_e32 v32, v16, v17
	v_max3_f32 v32, v32, v18, v19
	v_max3_f32 v32, v32, v20, v21
	v_max3_f32 v32, v32, v22, v23
	v_max3_f32 v32, v32, v24, v25
	v_max3_f32 v32, v32, v26, v27
	v_max3_f32 v32, v32, v28, v29
	v_max3_f32 v32, v32, v30, v31
	v_mov_b32_e32 v33, v32
	s_nop 1
	v_permlane32_swap_b32_e32 v32, v33
	v_max_f32_e32 v32, v32, v33
	v_fmamk_f32 v33, v32, 0x3dd53b94, v201
	v_fmamk_f32 v32, v32, 0x3dd53b94, v202
	v_max_f32_e32 v32, 0xf149f2ca, v32
	v_cmp_ge_f32_e32 vcc, s70, v33
	v_sub_f32_e32 v33, 0xf149f2ca, v32
	s_cmp_eq_u64 vcc, exec
	v_exp_f32_e32 v33, v33
	s_cselect_b64 vcc, -1, 0
	v_cndmask_b32_e32 v192, v32, v204, vcc
	v_pk_fma_f32 v[178:179], v[16:17], s[40:41], v[192:193] op_sel_hi:[1,0,0] neg_lo:[0,0,1] neg_hi:[0,0,1]
	v_mul_u32_u24_e32 v16, 0x50, v186
	v_pk_fma_f32 v[152:153], v[30:31], s[40:41], v[192:193] op_sel_hi:[1,0,0] neg_lo:[0,0,1] neg_hi:[0,0,1]
	v_pk_fma_f32 v[154:155], v[28:29], s[40:41], v[192:193] op_sel_hi:[1,0,0] neg_lo:[0,0,1] neg_hi:[0,0,1]
	v_pk_fma_f32 v[156:157], v[26:27], s[40:41], v[192:193] op_sel_hi:[1,0,0] neg_lo:[0,0,1] neg_hi:[0,0,1]
	v_pk_fma_f32 v[158:159], v[24:25], s[40:41], v[192:193] op_sel_hi:[1,0,0] neg_lo:[0,0,1] neg_hi:[0,0,1]
	v_pk_fma_f32 v[160:161], v[22:23], s[40:41], v[192:193] op_sel_hi:[1,0,0] neg_lo:[0,0,1] neg_hi:[0,0,1]
	v_pk_fma_f32 v[162:163], v[20:21], s[40:41], v[192:193] op_sel_hi:[1,0,0] neg_lo:[0,0,1] neg_hi:[0,0,1]
	v_pk_fma_f32 v[176:177], v[18:19], s[40:41], v[192:193] op_sel_hi:[1,0,0] neg_lo:[0,0,1] neg_hi:[0,0,1]
	v_cndmask_b32_e64 v88, v33, 1.0, vcc
	v_add3_u32 v211, s67, v16, v72
	s_add_i32 s17, s2, -2
	v_cmp_gt_u32_e64 s[2:3], 32, v64
	v_mov_b64_e32 v[30:31], v[14:15]
	v_mov_b64_e32 v[46:47], v[14:15]
	v_mov_b64_e32 v[78:79], v[14:15]
	v_mov_b32_e32 v117, v112
	v_mov_b32_e32 v118, v112
	v_mov_b32_e32 v119, v112
	v_lshlrev_b32_e32 v208, 2, v109
	v_mul_lo_u32 v215, v213, s65
	v_lshl_add_u32 v214, v109, 4, s79
	s_add_i32 s20, s74, -1
	v_lshl_add_u64 v[194:195], s[4:5], 0, v[190:191]
	v_lshl_add_u64 v[196:197], s[4:5], 0, v[188:189]
	v_lshl_add_u64 v[198:199], s[44:45], 0, v[104:105]
	s_mov_b32 s21, 0
	s_movk_i32 s22, 0x80
	v_mov_b64_e32 v[28:29], v[12:13]
	v_mov_b64_e32 v[26:27], v[10:11]
	v_mov_b64_e32 v[24:25], v[8:9]
	v_mov_b64_e32 v[22:23], v[6:7]
	v_mov_b64_e32 v[20:21], v[4:5]
	v_mov_b64_e32 v[18:19], v[2:3]
	v_mov_b64_e32 v[16:17], v[0:1]
	v_mov_b64_e32 v[44:45], v[12:13]
	v_mov_b64_e32 v[42:43], v[10:11]
	v_mov_b64_e32 v[40:41], v[8:9]
	v_mov_b64_e32 v[38:39], v[6:7]
	v_mov_b64_e32 v[36:37], v[4:5]
	v_mov_b64_e32 v[34:35], v[2:3]
	v_mov_b64_e32 v[32:33], v[0:1]
	v_mov_b64_e32 v[60:61], v[12:13]
	v_mov_b64_e32 v[58:59], v[10:11]
	v_mov_b64_e32 v[56:57], v[8:9]
	v_mov_b64_e32 v[54:55], v[6:7]
	v_mov_b64_e32 v[52:53], v[4:5]
	v_mov_b64_e32 v[50:51], v[2:3]
	v_mov_b64_e32 v[48:49], v[0:1]
	v_mov_b64_e32 v[76:77], v[12:13]
	v_mov_b64_e32 v[74:75], v[10:11]
	v_mov_b64_e32 v[72:73], v[8:9]
	v_mov_b64_e32 v[70:71], v[6:7]
	v_mov_b64_e32 v[68:69], v[4:5]
	v_mov_b64_e32 v[66:67], v[2:3]
	v_mov_b64_e32 v[64:65], v[0:1]
	s_add_i32 s18, s78, -2
	s_and_b32 s23, s18, 1
	s_lshl_b32 s24, s23, 15
	v_add_u32_e32 v248, s24, v216
	ds_read_b128 v[224:227], v248 offset:6656
	ds_read_b128 v[228:231], v248 offset:6672
	ds_read_b128 v[232:235], v248 offset:6720
	ds_read_b128 v[236:239], v248 offset:6736
	v_add_u32_e32 v248, v248, v217
	ds_read_b128 v[240:243], v248 offset:6784
	ds_read_b128 v[244:247], v248 offset:6816
	s_branch .LBB0_566

.LBB0_565:
	s_waitcnt lgkmcnt(4)
	v_mfma_f32_32x32x64_f8f6f4 v[96:111], v[96:103], v[120:127], 0
	v_cndmask_b32_e64 v176, v189, v192, s[4:5]
	v_fma_f32 v80, v80, s40, -v176
	v_fma_f32 v81, v81, s40, -v176
	v_fma_f32 v84, v84, s40, -v176
	v_fma_f32 v85, v85, s40, -v176
	v_fma_f32 v88, v88, s40, -v176
	v_fma_f32 v89, v89, s40, -v176
	v_fma_f32 v92, v92, s40, -v176
	v_fma_f32 v93, v93, s40, -v176
	v_exp_f32_e32 v80, v80
	v_exp_f32_e32 v81, v81
	v_exp_f32_e32 v84, v84
	v_exp_f32_e32 v85, v85
	v_exp_f32_e32 v88, v88
	v_exp_f32_e32 v89, v89
	s_waitcnt lgkmcnt(2)
	v_mfma_f32_32x32x64_f8f6f4 v[96:111], v[156:163], v[128:135], v[96:111]
	v_exp_f32_e32 v92, v92
	v_exp_f32_e32 v93, v93
	v_fma_f32 v82, v82, s40, -v176
	v_fma_f32 v83, v83, s40, -v176
	v_fma_f32 v86, v86, s40, -v176
	v_fma_f32 v87, v87, s40, -v176
	v_fma_f32 v90, v90, s40, -v176
	v_fma_f32 v91, v91, s40, -v176
	v_fma_f32 v94, v94, s40, -v176
	v_fma_f32 v95, v95, s40, -v176
	v_exp_f32_e32 v82, v82
	v_exp_f32_e32 v83, v83
	v_exp_f32_e32 v86, v86
	v_exp_f32_e32 v87, v87
	v_exp_f32_e32 v90, v90
	s_waitcnt lgkmcnt(0)
	v_mfma_f32_32x32x64_f8f6f4 v[96:111], v[148:155], v[136:143], v[96:111]
	v_lshl_add_u32 v240, s23, 14, v211
	ds_read_b128 v[224:227], v240
	ds_read_b128 v[228:231], v240 offset:16
	ds_read_b128 v[232:235], v240 offset:2560
	ds_read_b128 v[236:239], v240 offset:2576
	v_exp_f32_e32 v91, v91
	v_exp_f32_e32 v94, v94
	v_exp_f32_e32 v95, v95
	v_cvt_pk_fp8_f32 v148, v80, v81
	v_cvt_pk_fp8_f32 v149, v84, v85
	v_cvt_pk_fp8_f32 v150, v88, v89
	v_cvt_pk_fp8_f32 v151, v92, v93
	v_cvt_pk_fp8_f32 v148, v82, v83 op_sel:[0,0,1]
	v_cvt_pk_fp8_f32 v149, v86, v87 op_sel:[0,0,1]
	v_cvt_pk_fp8_f32 v150, v90, v91 op_sel:[0,0,1]
	v_cvt_pk_fp8_f32 v151, v94, v95 op_sel:[0,0,1]
	s_nop 0
	s_waitcnt lgkmcnt(2)
	v_mfma_f32_32x32x64_f8f6f4 v[48:63], v[144:151], v[224:231], v[48:63]
	ds_read_b128 v[80:83], v240 offset:5120
	ds_read_b128 v[84:87], v240 offset:5136
	ds_read_b128 v[152:155], v240 offset:7680
	ds_read_b128 v[156:159], v240 offset:7696
	s_waitcnt lgkmcnt(4)
	v_mfma_f32_32x32x64_f8f6f4 v[32:47], v[144:151], v[232:239], v[32:47]
	v_max_f32_e32 v88, v96, v97
	v_max3_f32 v88, v88, v98, v99
	v_max3_f32 v88, v88, v100, v101
	v_max3_f32 v88, v88, v102, v103
	v_max3_f32 v88, v88, v104, v105
	v_max3_f32 v88, v88, v106, v107
	s_waitcnt lgkmcnt(2)
	v_mfma_f32_32x32x64_f8f6f4 v[16:31], v[144:151], v[80:87], v[16:31]
	s_add_i32 s18, s78, -1
	s_and_b32 s23, s18, 1
	s_lshl_b32 s24, s23, 15
	v_add_u32_e32 v248, s24, v216
	ds_read_b128 v[224:227], v248 offset:6656
	ds_read_b128 v[228:231], v248 offset:6672
	ds_read_b128 v[232:235], v248 offset:6720
	ds_read_b128 v[236:239], v248 offset:6736
	v_add_u32_e32 v248, v248, v217
	ds_read_b128 v[240:243], v248 offset:6784
	ds_read_b128 v[244:247], v248 offset:6816
	v_max3_f32 v88, v88, v108, v109
	v_max3_f32 v88, v88, v110, v111
	v_mov_b32_e32 v89, v88
	s_nop 1
	v_permlane32_swap_b32_e32 v88, v89
	v_max_f32_e32 v80, v88, v89
	v_fma_f32 v81, v80, s40, -v176
	v_cmp_ge_f32_e32 vcc, s70, v81
	s_waitcnt lgkmcnt(6)
	v_mfma_f32_32x32x64_f8f6f4 v[0:15], v[144:151], v[152:159], v[0:15]
	s_cmp_eq_u64 vcc, exec
	s_cbranch_scc0 .Lmla_rare_a0
	v_mov_b32_e32 v192, v176
	v_mov_b32_e32 v88, 1.0

.LBB0_570:
	s_waitcnt lgkmcnt(4)
	v_mfma_f32_32x32x64_f8f6f4 v[80:95], v[224:231], v[120:127], 0
	s_mov_b64 s[4:5], exec
	s_cmp_ge_u32 s18, s20
	s_waitcnt lgkmcnt(2)
	v_mfma_f32_32x32x64_f8f6f4 v[80:95], v[232:239], v[128:135], v[80:95]
	s_waitcnt lgkmcnt(0)
	v_mfma_f32_32x32x64_f8f6f4 v[80:95], v[240:247], v[136:143], v[80:95]
	s_nop 15
	s_nop 3
	v_max_f32_e32 v96, v80, v81
	v_max3_f32 v96, v96, v82, v83
	v_max3_f32 v96, v96, v84, v85
	v_max3_f32 v96, v96, v86, v87
	v_max3_f32 v96, v96, v88, v89
	v_max3_f32 v96, v96, v90, v91
	v_max3_f32 v96, v96, v92, v93
	v_max3_f32 v96, v96, v94, v95
	v_mov_b32_e32 v97, v96
	s_nop 1
	v_permlane32_swap_b32_e32 v96, v97
	v_max_f32_e32 v96, v96, v97
	v_fma_f32 v97, v96, s40, -v192
	v_cmp_ge_f32_e32 vcc, s70, v97
	s_cbranch_scc1 .LBB0_577
	s_xor_b32 s25, s23, 1
	s_lshl_b32 s18, s25, 15
	s_add_i32 s26, s18, 0
	v_add3_u32 v97, s26, v212, v190
	s_waitcnt vmcnt(1)
	ds_write_b128 v97, v[168:171]
	s_and_saveexec_b64 s[18:19], s[0:1]
	v_add3_u32 v97, s26, v215, v188
	ds_write_b128 v97, v[164:167]
	s_or_b64 exec, exec, s[18:19]
	v_lshl_add_u32 v97, s25, 14, v207
	s_cmp_ge_u32 s78, s74
	s_waitcnt vmcnt(0)
	ds_write_b128 v97, v[172:175]
	s_cbranch_scc1 .LBB0_577
	s_cmp_lt_u32 s78, s77
	s_cselect_b32 s18, 0, s77
	s_cselect_b32 s19, s76, s75
	s_lshl_b32 s18, s18, 6
	s_sub_i32 s25, s19, s18
	s_add_i32 s25, s25, s22
	v_add_u32_e32 v97, s25, v210
	v_mad_i64_i32 v[98:99], s[18:19], v97, s64, v[194:195]
	global_load_dwordx4 v[168:171], v[98:99], off
	s_and_saveexec_b64 s[18:19], s[0:1]
	s_cbranch_execz .LBB0_576
	v_add_u32_e32 v97, s25, v213
	v_mad_i64_i32 v[98:99], s[26:27], v97, s64, v[196:197]
	global_load_dwordx4 v[164:167], v[98:99], off

.LBB0_1873:
	s_or_b64 exec, exec, s[2:3]
	v_mul_f32_e32 v0, v106, v0
	v_mul_f32_e32 v1, v106, v1
	v_mul_f32_e32 v26, v106, v26
	v_mul_f32_e32 v0, v0, v113
	v_mul_f32_e32 v1, v1, v112
	v_mul_f32_e32 v26, v26, v135
	v_med3_f32 v0, v0, s67, v205
	v_med3_f32 v1, v1, s67, v205
	v_mov_b32_e32 v135, v187
	v_cvt_pk_fp8_f32 v135, v0, v1
	v_mul_f32_e32 v2, v106, v2
	v_mul_f32_e32 v3, v106, v3
	v_mul_f32_e32 v2, v2, v111
	v_mul_f32_e32 v3, v3, v110
	v_med3_f32 v0, v2, s67, v205
	v_med3_f32 v1, v3, s67, v205
	v_mul_f32_e32 v25, v106, v25
	v_cvt_pk_fp8_f32 v135, v0, v1 op_sel:[0,0,1]
	v_max_f32_e32 v0, v104, v104
	v_max_f32_e32 v1, v105, v105
	v_mul_f32_e32 v25, v25, v136
	v_med3_f32 v0, v0, s67, v205
	v_med3_f32 v1, v1, s67, v205
	v_mov_b32_e32 v136, v187
	v_cvt_pk_fp8_f32 v136, v0, v1
	v_max_f32_e32 v2, v100, v100
	v_max_f32_e32 v1, v101, v101
	v_med3_f32 v0, v2, s67, v205
	v_med3_f32 v1, v1, s67, v205
	v_mul_f32_e32 v24, v106, v24
	v_cvt_pk_fp8_f32 v136, v0, v1 op_sel:[0,0,1]
	v_max_f32_e32 v0, v98, v98
	v_max_f32_e32 v1, v99, v99
	v_mul_f32_e32 v24, v24, v137
	v_med3_f32 v0, v0, s67, v205
	v_med3_f32 v1, v1, s67, v205
	v_mov_b32_e32 v137, v187
	v_cvt_pk_fp8_f32 v137, v0, v1
	v_max_f32_e32 v2, v96, v96
	v_max_f32_e32 v1, v97, v97
	v_med3_f32 v0, v2, s67, v205
	v_med3_f32 v1, v1, s67, v205
	v_mul_f32_e32 v31, v106, v31
	v_cvt_pk_fp8_f32 v137, v0, v1 op_sel:[0,0,1]
	v_max_f32_e32 v0, v94, v94
	v_max_f32_e32 v1, v95, v95
	v_mul_f32_e32 v31, v31, v138
	v_med3_f32 v0, v0, s67, v205
	v_med3_f32 v1, v1, s67, v205
	v_mov_b32_e32 v138, v187
	v_cvt_pk_fp8_f32 v138, v0, v1
	v_max_f32_e32 v2, v92, v92
	v_max_f32_e32 v1, v93, v93
	v_med3_f32 v0, v2, s67, v205
	v_med3_f32 v1, v1, s67, v205
	v_mul_f32_e32 v30, v106, v30
	v_cvt_pk_fp8_f32 v138, v0, v1 op_sel:[0,0,1]
	v_max_f32_e32 v0, v90, v90
	v_max_f32_e32 v1, v91, v91
	v_mul_f32_e32 v30, v30, v139
	v_med3_f32 v0, v0, s67, v205
	v_med3_f32 v1, v1, s67, v205
	v_mov_b32_e32 v139, v187
	v_cvt_pk_fp8_f32 v139, v0, v1
	v_max_f32_e32 v2, v88, v88
	v_max_f32_e32 v1, v89, v89
	v_med3_f32 v0, v2, s67, v205
	v_med3_f32 v1, v1, s67, v205
	v_mul_f32_e32 v29, v106, v29
	v_cvt_pk_fp8_f32 v139, v0, v1 op_sel:[0,0,1]
	v_max_f32_e32 v0, v86, v86
	v_max_f32_e32 v1, v87, v87
	v_mul_f32_e32 v29, v29, v140
	v_med3_f32 v0, v0, s67, v205
	v_med3_f32 v1, v1, s67, v205
	v_mov_b32_e32 v140, v187
	v_cvt_pk_fp8_f32 v140, v0, v1
	v_max_f32_e32 v2, v84, v84
	v_max_f32_e32 v1, v85, v85
	v_med3_f32 v0, v2, s67, v205
	v_med3_f32 v1, v1, s67, v205
	v_mul_f32_e32 v28, v106, v28
	v_cvt_pk_fp8_f32 v140, v0, v1 op_sel:[0,0,1]
	v_max_f32_e32 v0, v82, v82
	v_max_f32_e32 v1, v83, v83
	v_mul_f32_e32 v28, v28, v141
	v_med3_f32 v0, v0, s67, v205
	v_med3_f32 v1, v1, s67, v205
	v_mov_b32_e32 v141, v187
	v_cvt_pk_fp8_f32 v141, v0, v1
	v_max_f32_e32 v2, v80, v80
	v_max_f32_e32 v1, v81, v81
	v_med3_f32 v0, v2, s67, v205
	v_med3_f32 v1, v1, s67, v205
	v_mul_f32_e32 v35, v106, v35
	v_cvt_pk_fp8_f32 v141, v0, v1 op_sel:[0,0,1]
	v_max_f32_e32 v0, v78, v78
	v_max_f32_e32 v1, v79, v79
	v_mul_f32_e32 v35, v35, v142
	v_med3_f32 v0, v0, s67, v205
	v_med3_f32 v1, v1, s67, v205
	v_mov_b32_e32 v142, v187
	v_cvt_pk_fp8_f32 v142, v0, v1
	v_mul_f32_e32 v8, v106, v8
	v_mul_f32_e32 v9, v106, v9
	v_mul_f32_e32 v4, v106, v4
	v_mul_f32_e32 v5, v106, v5
	v_mul_f32_e32 v60, v60, v106
	v_mul_f32_e32 v61, v61, v106
	v_mul_f32_e32 v56, v56, v106
	v_mul_f32_e32 v57, v57, v106
	v_mul_f32_e32 v52, v52, v106
	v_mul_f32_e32 v53, v106, v53
	v_mul_f32_e32 v48, v106, v48
	v_mul_f32_e32 v49, v106, v49
	v_mul_f32_e32 v44, v106, v44
	v_mul_f32_e32 v45, v106, v45
	v_mul_f32_e32 v40, v106, v40
	v_mul_f32_e32 v41, v106, v41
	v_mul_f32_e32 v36, v106, v36
	v_mul_f32_e32 v37, v106, v37
	v_mul_f32_e32 v32, v106, v32
	v_mul_f32_e32 v33, v106, v33
	v_mul_f32_e32 v27, v106, v27
	v_mul_f32_e32 v20, v106, v20
	v_mul_f32_e32 v8, v8, v121
	v_mul_f32_e32 v9, v9, v120
	v_mul_f32_e32 v4, v4, v117
	v_mul_f32_e32 v5, v5, v116
	v_max_f32_e32 v2, v76, v76
	v_max_f32_e32 v1, v77, v77
	v_mul_f32_e32 v60, v60, v181
	v_mul_f32_e32 v61, v61, v180
	v_mul_f32_e32 v56, v56, v177
	v_mul_f32_e32 v57, v57, v176
	v_mul_f32_e32 v52, v52, v173
	v_mul_f32_e32 v53, v53, v172
	v_mul_f32_e32 v48, v48, v161
	v_mul_f32_e32 v49, v49, v160
	v_mul_f32_e32 v44, v44, v157
	v_mul_f32_e32 v45, v45, v156
	v_mul_f32_e32 v40, v40, v153
	v_mul_f32_e32 v41, v41, v152
	v_mul_f32_e32 v36, v36, v149
	v_mul_f32_e32 v37, v37, v148
	v_mul_f32_e32 v32, v32, v145
	v_mul_f32_e32 v33, v33, v144
	v_mul_f32_e32 v27, v27, v134
	v_mul_f32_e32 v20, v20, v133
	v_mul_f32_e32 v18, v106, v18
	v_mul_f32_e32 v19, v106, v19
	v_mul_f32_e32 v12, v106, v12
	v_mul_f32_e32 v13, v106, v13
	v_mul_f32_e32 v14, v106, v14
	v_mul_f32_e32 v15, v106, v15
	v_med3_f32 v8, v8, s67, v205
	v_med3_f32 v9, v9, s67, v205
	v_mov_b32_e32 v133, v187
	v_med3_f32 v4, v4, s67, v205
	v_med3_f32 v5, v5, s67, v205
	v_mov_b32_e32 v134, v187
	v_med3_f32 v0, v2, s67, v205
	v_med3_f32 v1, v1, s67, v205
	v_mul_f32_e32 v34, v106, v34
	v_mul_f32_e32 v18, v18, v127
	v_mul_f32_e32 v19, v19, v126
	v_mul_f32_e32 v12, v12, v125
	v_mul_f32_e32 v13, v13, v124
	v_mul_f32_e32 v14, v14, v123
	v_mul_f32_e32 v15, v15, v122
	v_med3_f32 v60, v60, s67, v205
	v_med3_f32 v61, v61, s67, v205
	v_mov_b32_e32 v120, v187
	v_med3_f32 v56, v56, s67, v205
	v_med3_f32 v57, v57, s67, v205
	v_mov_b32_e32 v121, v187
	v_med3_f32 v52, v52, s67, v205
	v_med3_f32 v53, v53, s67, v205
	v_mov_b32_e32 v122, v187
	v_med3_f32 v48, v48, s67, v205
	v_med3_f32 v49, v49, s67, v205
	v_mov_b32_e32 v123, v187
	v_med3_f32 v44, v44, s67, v205
	v_med3_f32 v45, v45, s67, v205
	v_mov_b32_e32 v124, v187
	v_med3_f32 v40, v40, s67, v205
	v_med3_f32 v41, v41, s67, v205
	v_mov_b32_e32 v125, v187
	v_med3_f32 v36, v36, s67, v205
	v_med3_f32 v37, v37, s67, v205
	v_mov_b32_e32 v126, v187
	v_med3_f32 v32, v32, s67, v205
	v_med3_f32 v33, v33, s67, v205
	v_mov_b32_e32 v127, v187
	v_cvt_pk_fp8_f32 v133, v8, v9
	v_cvt_pk_fp8_f32 v134, v4, v5
	v_cvt_pk_fp8_f32 v142, v0, v1 op_sel:[0,0,1]
	v_max_f32_e32 v0, v74, v74
	v_max_f32_e32 v1, v75, v75
	s_and_b32 s2, s18, 0x3fffffc0
	v_mul_f32_e32 v34, v34, v143
	v_mul_f32_e32 v10, v106, v10
	v_mul_f32_e32 v11, v106, v11
	v_mul_f32_e32 v6, v106, v6
	v_mul_f32_e32 v7, v106, v7
	v_cvt_pk_fp8_f32 v120, v60, v61
	v_cvt_pk_fp8_f32 v121, v56, v57
	v_cvt_pk_fp8_f32 v122, v52, v53
	v_cvt_pk_fp8_f32 v123, v48, v49
	v_cvt_pk_fp8_f32 v124, v44, v45
	v_cvt_pk_fp8_f32 v125, v40, v41
	v_cvt_pk_fp8_f32 v126, v36, v37
	v_cvt_pk_fp8_f32 v127, v32, v33
	v_med3_f32 v0, v0, s67, v205
	v_med3_f32 v1, v1, s67, v205
	v_mov_b32_e32 v143, v187
	s_lshl_b32 s2, s2, 2
	v_mul_f32_e32 v62, v62, v106
	v_mul_f32_e32 v63, v63, v106
	v_mul_f32_e32 v58, v58, v106
	v_mul_f32_e32 v59, v59, v106
	v_mul_f32_e32 v54, v106, v54
	v_mul_f32_e32 v55, v106, v55
	v_mul_f32_e32 v50, v106, v50
	v_mul_f32_e32 v51, v106, v51
	v_mul_f32_e32 v46, v106, v46
	v_mul_f32_e32 v47, v106, v47
	v_mul_f32_e32 v42, v106, v42
	v_mul_f32_e32 v43, v106, v43
	v_mul_f32_e32 v38, v106, v38
	v_mul_f32_e32 v39, v106, v39
	v_mul_f32_e32 v21, v106, v21
	v_mul_f32_e32 v16, v106, v16
	v_mul_f32_e32 v17, v106, v17
	v_mul_f32_e32 v10, v10, v119
	v_mul_f32_e32 v11, v11, v118
	v_mul_f32_e32 v6, v6, v115
	v_mul_f32_e32 v7, v7, v114
	v_cvt_pk_fp8_f32 v143, v0, v1
	v_mul_u32_u24_e32 v0, 0xd0, v188
	s_add_i32 s2, s2, 0
	v_mul_f32_e32 v62, v62, v179
	v_mul_f32_e32 v63, v63, v178
	v_mul_f32_e32 v58, v58, v175
	v_mul_f32_e32 v59, v59, v174
	v_mul_f32_e32 v54, v54, v163
	v_mul_f32_e32 v55, v55, v162
	v_mul_f32_e32 v50, v50, v159
	v_mul_f32_e32 v51, v51, v158
	v_mul_f32_e32 v46, v46, v155
	v_mul_f32_e32 v47, v47, v154
	v_mul_f32_e32 v42, v42, v151
	v_mul_f32_e32 v43, v43, v150
	v_mul_f32_e32 v38, v38, v147
	v_mul_f32_e32 v39, v39, v146
	v_mul_f32_e32 v21, v21, v132
	v_mul_f32_e32 v22, v106, v22
	v_mul_f32_e32 v23, v106, v23
	v_mul_f32_e32 v16, v16, v129
	v_mul_f32_e32 v17, v17, v128
	v_med3_f32 v8, v10, s67, v205
	v_med3_f32 v9, v11, s67, v205
	v_med3_f32 v6, v6, s67, v205
	v_med3_f32 v7, v7, s67, v205
	v_max_f32_e32 v2, v72, v72
	v_add3_u32 v214, 0, v0, v186
	s_add_i32 s77, s2, 0x18000
	s_ashr_i32 s2, s19, 6
	v_mul_f32_e32 v22, v22, v131
	v_mul_f32_e32 v23, v23, v130
	v_med3_f32 v62, v62, s67, v205
	v_med3_f32 v63, v63, s67, v205
	v_med3_f32 v56, v58, s67, v205
	v_med3_f32 v57, v59, s67, v205
	v_med3_f32 v54, v54, s67, v205
	v_med3_f32 v55, v55, s67, v205
	v_med3_f32 v48, v50, s67, v205
	v_med3_f32 v49, v51, s67, v205
	v_med3_f32 v46, v46, s67, v205
	v_med3_f32 v47, v47, s67, v205
	v_med3_f32 v40, v42, s67, v205
	v_med3_f32 v41, v43, s67, v205
	v_med3_f32 v38, v38, s67, v205
	v_med3_f32 v39, v39, s67, v205
	v_med3_f32 v32, v34, s67, v205
	v_med3_f32 v33, v35, s67, v205
	v_med3_f32 v28, v28, s67, v205
	v_med3_f32 v29, v29, s67, v205
	v_mov_b32_e32 v128, v187
	v_med3_f32 v24, v24, s67, v205
	v_med3_f32 v25, v25, s67, v205
	v_mov_b32_e32 v129, v187
	v_med3_f32 v20, v20, s67, v205
	v_med3_f32 v21, v21, s67, v205
	v_mov_b32_e32 v130, v187
	v_med3_f32 v16, v16, s67, v205
	v_med3_f32 v17, v17, s67, v205
	v_mov_b32_e32 v131, v187
	v_cvt_pk_fp8_f32 v133, v8, v9 op_sel:[0,0,1]
	v_cvt_pk_fp8_f32 v134, v6, v7 op_sel:[0,0,1]
	v_med3_f32 v8, v2, s67, v205
	ds_read_b128 v[0:3], v214
	ds_read_b128 v[4:7], v214 offset:16
	s_lshl_b32 s75, s17, 8
	s_ashr_i32 s3, s2, 31
	v_cvt_pk_fp8_f32 v120, v62, v63 op_sel:[0,0,1]
	v_cvt_pk_fp8_f32 v121, v56, v57 op_sel:[0,0,1]
	v_cvt_pk_fp8_f32 v122, v54, v55 op_sel:[0,0,1]
	v_cvt_pk_fp8_f32 v123, v48, v49 op_sel:[0,0,1]
	v_cvt_pk_fp8_f32 v124, v46, v47 op_sel:[0,0,1]
	v_cvt_pk_fp8_f32 v125, v40, v41 op_sel:[0,0,1]
	v_cvt_pk_fp8_f32 v126, v38, v39 op_sel:[0,0,1]
	v_cvt_pk_fp8_f32 v127, v32, v33 op_sel:[0,0,1]
	v_cvt_pk_fp8_f32 v128, v28, v29
	v_cvt_pk_fp8_f32 v129, v24, v25
	v_cvt_pk_fp8_f32 v130, v20, v21
	v_cvt_pk_fp8_f32 v131, v16, v17
	s_addk_i32 s75, 0x2000
	s_lshl_b64 s[2:3], s[2:3], 16
	v_max_f32_e32 v9, v73, v73
	s_add_u32 s2, s40, s2
	v_med3_f32 v9, v9, s67, v205
	s_addc_u32 s3, s41, s3
	v_med3_f32 v30, v30, s67, v205
	v_med3_f32 v31, v31, s67, v205
	v_med3_f32 v24, v26, s67, v205
	v_med3_f32 v25, v27, s67, v205
	v_med3_f32 v22, v22, s67, v205
	v_med3_f32 v23, v23, s67, v205
	v_med3_f32 v16, v18, s67, v205
	v_med3_f32 v17, v19, s67, v205
	v_cvt_pk_fp8_f32 v143, v8, v9 op_sel:[0,0,1]
	v_lshl_add_u64 v[8:9], s[2:3], 0, v[102:103]
	v_cvt_pk_fp8_f32 v128, v30, v31 op_sel:[0,0,1]
	v_cvt_pk_fp8_f32 v129, v24, v25 op_sel:[0,0,1]
	v_cvt_pk_fp8_f32 v130, v22, v23 op_sel:[0,0,1]
	v_cvt_pk_fp8_f32 v131, v16, v17 op_sel:[0,0,1]
	s_waitcnt lgkmcnt(0)
	v_mfma_f32_32x32x64_f8f6f4 v[16:31], v[0:7], v[120:127], 0
	ds_read_b128 v[0:3], v214 offset:64
	ds_read_b128 v[4:7], v214 offset:80
	global_load_dwordx4 v[172:175], v[8:9], off
	v_med3_f32 v12, v12, s67, v205
	v_med3_f32 v13, v13, s67, v205
	v_mov_b32_e32 v132, v187
	v_cvt_pk_fp8_f32 v132, v12, v13
	v_med3_f32 v14, v14, s67, v205
	v_med3_f32 v15, v15, s67, v205
	s_mov_b32 s17, s16
	v_cvt_pk_fp8_f32 v132, v14, v15 op_sel:[0,0,1]
	s_mov_b32 s18, s16
	s_mov_b32 s19, s16
	s_mov_b32 s20, s16
	s_mov_b32 s21, s16
	s_mov_b32 s22, s16
	s_waitcnt lgkmcnt(0)
	v_mfma_f32_32x32x64_f8f6f4 v[16:31], v[0:7], v[128:135], v[16:31]
	v_sub_u32_e32 v0, v214, v108
	ds_read_b128 v[32:35], v0 offset:128
	ds_read_b128 v[36:39], v0 offset:160
	s_mov_b32 s23, s16
	s_mov_b32 s24, s16
	s_mov_b32 s25, s16
	s_mov_b32 s26, s16
	s_mov_b32 s27, s16
	s_mov_b32 s28, s16
	s_mov_b32 s29, s16
	s_mov_b32 s30, s16
	s_mov_b32 s31, s16
	v_mov_b64_e32 v[0:1], s[16:17]
	v_and_b32_e32 v64, 63, v109
	v_mov_b64_e32 v[14:15], s[30:31]
	v_mov_b64_e32 v[2:3], s[18:19]
	s_waitcnt lgkmcnt(0)
	v_mfma_f32_32x32x64_f8f6f4 v[16:31], v[32:39], v[136:143], v[16:31]
	v_mov_b64_e32 v[4:5], s[20:21]
	v_mov_b64_e32 v[6:7], s[22:23]
	v_mov_b64_e32 v[8:9], s[24:25]
	v_mov_b64_e32 v[10:11], s[26:27]
	v_mov_b64_e32 v[12:13], s[28:29]
	v_mov_b32_e32 v112, 0x38383838
	v_cmp_gt_u32_e64 s[2:3], 32, v64
	v_mov_b64_e32 v[62:63], v[14:15]
	v_mov_b64_e32 v[78:79], v[14:15]
	s_mov_b32 s76, 2
	v_sub_u32_e32 v215, 0, v108
	v_lshl_add_u32 v208, v188, 2, s77
	v_mov_b32_e32 v113, v112
	v_mov_b32_e32 v114, v112
	s_nop 5
	v_max_f32_e32 v32, v16, v17
	v_max3_f32 v32, v32, v18, v19
	v_max3_f32 v32, v32, v20, v21
	v_max3_f32 v32, v32, v22, v23
	v_max3_f32 v32, v32, v24, v25
	v_max3_f32 v32, v32, v26, v27
	v_max3_f32 v32, v32, v28, v29
	v_max3_f32 v32, v32, v30, v31
	v_mov_b32_e32 v33, v32
	s_nop 1
	v_permlane32_swap_b32_e32 v32, v33
	v_max_f32_e32 v32, v32, v33
	v_fmamk_f32 v33, v32, 0x3dd53b94, v203
	v_fmamk_f32 v32, v32, 0x3dd53b94, v204
	v_max_f32_e32 v32, 0xf149f2ca, v32
	v_cmp_ge_f32_e32 vcc, s68, v33
	v_sub_f32_e32 v33, 0xf149f2ca, v32
	s_cmp_eq_u64 vcc, exec
	v_exp_f32_e32 v33, v33
	s_cselect_b64 vcc, -1, 0
	v_cndmask_b32_e32 v194, v32, v206, vcc
	v_pk_fma_f32 v[178:179], v[16:17], s[38:39], v[194:195] op_sel_hi:[1,0,0] neg_lo:[0,0,1] neg_hi:[0,0,1]
	v_mul_u32_u24_e32 v16, 0x50, v188
	v_pk_fma_f32 v[152:153], v[30:31], s[38:39], v[194:195] op_sel_hi:[1,0,0] neg_lo:[0,0,1] neg_hi:[0,0,1]
	v_pk_fma_f32 v[154:155], v[28:29], s[38:39], v[194:195] op_sel_hi:[1,0,0] neg_lo:[0,0,1] neg_hi:[0,0,1]
	v_pk_fma_f32 v[156:157], v[26:27], s[38:39], v[194:195] op_sel_hi:[1,0,0] neg_lo:[0,0,1] neg_hi:[0,0,1]
	v_pk_fma_f32 v[158:159], v[24:25], s[38:39], v[194:195] op_sel_hi:[1,0,0] neg_lo:[0,0,1] neg_hi:[0,0,1]
	v_pk_fma_f32 v[160:161], v[22:23], s[38:39], v[194:195] op_sel_hi:[1,0,0] neg_lo:[0,0,1] neg_hi:[0,0,1]
	v_pk_fma_f32 v[162:163], v[20:21], s[38:39], v[194:195] op_sel_hi:[1,0,0] neg_lo:[0,0,1] neg_hi:[0,0,1]
	v_pk_fma_f32 v[176:177], v[18:19], s[38:39], v[194:195] op_sel_hi:[1,0,0] neg_lo:[0,0,1] neg_hi:[0,0,1]
	v_cndmask_b32_e64 v88, v33, 1.0, vcc
	v_add3_u32 v209, s65, v16, v186
	v_mov_b64_e32 v[30:31], v[14:15]
	v_mov_b64_e32 v[46:47], v[14:15]
	v_mov_b32_e32 v115, v112
	v_mov_b32_e32 v116, v112
	v_mov_b32_e32 v117, v112
	v_mov_b32_e32 v118, v112
	v_mov_b32_e32 v119, v112
	v_lshlrev_b32_e32 v186, 2, v107
	v_mul_lo_u32 v216, v212, s63
	v_lshl_add_u32 v213, v107, 4, s77
	v_lshl_add_u64 v[196:197], s[4:5], 0, v[190:191]
	v_lshl_add_u64 v[198:199], s[4:5], 0, v[192:193]
	v_lshl_add_u64 v[200:201], s[40:41], 0, v[102:103]
	s_mov_b32 s17, 0
	v_mov_b64_e32 v[28:29], v[12:13]
	v_mov_b64_e32 v[26:27], v[10:11]
	v_mov_b64_e32 v[24:25], v[8:9]
	v_mov_b64_e32 v[22:23], v[6:7]
	v_mov_b64_e32 v[20:21], v[4:5]
	v_mov_b64_e32 v[18:19], v[2:3]
	v_mov_b64_e32 v[16:17], v[0:1]
	v_mov_b64_e32 v[44:45], v[12:13]
	v_mov_b64_e32 v[42:43], v[10:11]
	v_mov_b64_e32 v[40:41], v[8:9]
	v_mov_b64_e32 v[38:39], v[6:7]
	v_mov_b64_e32 v[36:37], v[4:5]
	v_mov_b64_e32 v[34:35], v[2:3]
	v_mov_b64_e32 v[32:33], v[0:1]
	v_mov_b64_e32 v[60:61], v[12:13]
	v_mov_b64_e32 v[58:59], v[10:11]
	v_mov_b64_e32 v[56:57], v[8:9]
	v_mov_b64_e32 v[54:55], v[6:7]
	v_mov_b64_e32 v[52:53], v[4:5]
	v_mov_b64_e32 v[50:51], v[2:3]
	v_mov_b64_e32 v[48:49], v[0:1]
	v_mov_b64_e32 v[76:77], v[12:13]
	v_mov_b64_e32 v[74:75], v[10:11]
	v_mov_b64_e32 v[72:73], v[8:9]
	v_mov_b64_e32 v[70:71], v[6:7]
	v_mov_b64_e32 v[68:69], v[4:5]
	v_mov_b64_e32 v[66:67], v[2:3]
	v_mov_b64_e32 v[64:65], v[0:1]
	s_add_i32 s98, s76, -2
	s_and_b32 s24, s98, 1
	s_lshl_b32 s25, s24, 15
	v_add_u32_e32 v248, s25, v214
	ds_read_b128 v[224:227], v248 offset:6656
	ds_read_b128 v[228:231], v248 offset:6672
	ds_read_b128 v[232:235], v248 offset:6720
	ds_read_b128 v[236:239], v248 offset:6736
	v_add_u32_e32 v248, v248, v215
	ds_read_b128 v[240:243], v248 offset:6784
	ds_read_b128 v[244:247], v248 offset:6816
	s_branch .LBB0_1876

.LBB0_1875:
	s_waitcnt lgkmcnt(4)
	v_mfma_f32_32x32x64_f8f6f4 v[96:111], v[96:103], v[120:127], 0
	v_cndmask_b32_e64 v176, v191, v194, s[4:5]
	v_fma_f32 v80, v80, s38, -v176
	v_fma_f32 v81, v81, s38, -v176
	v_fma_f32 v84, v84, s38, -v176
	v_fma_f32 v85, v85, s38, -v176
	v_fma_f32 v88, v88, s38, -v176
	v_fma_f32 v89, v89, s38, -v176
	v_fma_f32 v92, v92, s38, -v176
	v_fma_f32 v93, v93, s38, -v176
	v_exp_f32_e32 v80, v80
	v_exp_f32_e32 v81, v81
	v_exp_f32_e32 v84, v84
	v_exp_f32_e32 v85, v85
	v_exp_f32_e32 v88, v88
	v_exp_f32_e32 v89, v89
	s_waitcnt lgkmcnt(2)
	v_mfma_f32_32x32x64_f8f6f4 v[96:111], v[156:163], v[128:135], v[96:111]
	v_exp_f32_e32 v92, v92
	v_exp_f32_e32 v93, v93
	v_fma_f32 v82, v82, s38, -v176
	v_fma_f32 v83, v83, s38, -v176
	v_fma_f32 v86, v86, s38, -v176
	v_fma_f32 v87, v87, s38, -v176
	v_fma_f32 v90, v90, s38, -v176
	v_fma_f32 v91, v91, s38, -v176
	v_fma_f32 v94, v94, s38, -v176
	v_fma_f32 v95, v95, s38, -v176
	v_exp_f32_e32 v82, v82
	v_exp_f32_e32 v83, v83
	v_exp_f32_e32 v86, v86
	v_exp_f32_e32 v87, v87
	v_exp_f32_e32 v90, v90
	s_waitcnt lgkmcnt(0)
	v_mfma_f32_32x32x64_f8f6f4 v[96:111], v[148:155], v[136:143], v[96:111]
	v_lshl_add_u32 v240, s24, 14, v209
	ds_read_b128 v[224:227], v240
	ds_read_b128 v[228:231], v240 offset:16
	ds_read_b128 v[232:235], v240 offset:2560
	ds_read_b128 v[236:239], v240 offset:2576
	v_exp_f32_e32 v91, v91
	v_exp_f32_e32 v94, v94
	v_exp_f32_e32 v95, v95
	v_cvt_pk_fp8_f32 v148, v80, v81
	v_cvt_pk_fp8_f32 v149, v84, v85
	v_cvt_pk_fp8_f32 v150, v88, v89
	v_cvt_pk_fp8_f32 v151, v92, v93
	v_cvt_pk_fp8_f32 v148, v82, v83 op_sel:[0,0,1]
	v_cvt_pk_fp8_f32 v149, v86, v87 op_sel:[0,0,1]
	v_cvt_pk_fp8_f32 v150, v90, v91 op_sel:[0,0,1]
	v_cvt_pk_fp8_f32 v151, v94, v95 op_sel:[0,0,1]
	s_nop 0
	s_waitcnt lgkmcnt(2)
	v_mfma_f32_32x32x64_f8f6f4 v[48:63], v[144:151], v[224:231], v[48:63]
	ds_read_b128 v[80:83], v240 offset:5120
	ds_read_b128 v[84:87], v240 offset:5136
	ds_read_b128 v[152:155], v240 offset:7680
	ds_read_b128 v[156:159], v240 offset:7696
	s_waitcnt lgkmcnt(4)
	v_mfma_f32_32x32x64_f8f6f4 v[32:47], v[144:151], v[232:239], v[32:47]
	v_max_f32_e32 v88, v96, v97
	v_max3_f32 v88, v88, v98, v99
	v_max3_f32 v88, v88, v100, v101
	v_max3_f32 v88, v88, v102, v103
	v_max3_f32 v88, v88, v104, v105
	v_max3_f32 v88, v88, v106, v107
	s_waitcnt lgkmcnt(2)
	v_mfma_f32_32x32x64_f8f6f4 v[16:31], v[144:151], v[80:87], v[16:31]
	s_add_i32 s98, s76, -1
	s_and_b32 s24, s98, 1
	s_lshl_b32 s25, s24, 15
	v_add_u32_e32 v248, s25, v214
	ds_read_b128 v[224:227], v248 offset:6656
	ds_read_b128 v[228:231], v248 offset:6672
	ds_read_b128 v[232:235], v248 offset:6720
	ds_read_b128 v[236:239], v248 offset:6736
	v_add_u32_e32 v248, v248, v215
	ds_read_b128 v[240:243], v248 offset:6784
	ds_read_b128 v[244:247], v248 offset:6816
	v_max3_f32 v88, v88, v108, v109
	v_max3_f32 v88, v88, v110, v111
	v_mov_b32_e32 v89, v88
	s_nop 1
	v_permlane32_swap_b32_e32 v88, v89
	v_max_f32_e32 v80, v88, v89
	v_fma_f32 v81, v80, s38, -v176
	v_cmp_ge_f32_e32 vcc, s68, v81
	s_waitcnt lgkmcnt(6)
	v_mfma_f32_32x32x64_f8f6f4 v[0:15], v[144:151], v[152:159], v[0:15]
	s_cmp_eq_u64 vcc, exec
	s_cbranch_scc0 .Lmla_rare_a1
	v_mov_b32_e32 v194, v176
	v_mov_b32_e32 v88, 1.0

.LBB0_1880:
	s_waitcnt lgkmcnt(4)
	v_mfma_f32_32x32x64_f8f6f4 v[80:95], v[224:231], v[120:127], 0
	s_xor_b32 s22, s24, 1
	s_lshl_b32 s18, s22, 15
	s_add_i32 s23, s18, 0
	s_mov_b64 s[20:21], exec
	s_waitcnt lgkmcnt(2)
	v_mfma_f32_32x32x64_f8f6f4 v[80:95], v[232:239], v[128:135], v[80:95]
	s_waitcnt lgkmcnt(0)
	v_mfma_f32_32x32x64_f8f6f4 v[80:95], v[240:247], v[136:143], v[80:95]
	s_nop 15
	s_nop 3
	v_max_f32_e32 v96, v80, v81
	v_max3_f32 v96, v96, v82, v83
	v_max3_f32 v96, v96, v84, v85
	v_max3_f32 v96, v96, v86, v87
	v_max3_f32 v96, v96, v88, v89
	v_max3_f32 v96, v96, v90, v91
	v_max3_f32 v96, v96, v92, v93
	v_max3_f32 v96, v96, v94, v95
	v_mov_b32_e32 v97, v96
	s_nop 1
	v_permlane32_swap_b32_e32 v96, v97
	v_max_f32_e32 v96, v96, v97
	v_fma_f32 v97, v96, s38, -v194
	v_cmp_ge_f32_e64 s[4:5], s68, v97
	v_add3_u32 v97, s23, v210, v190
	s_waitcnt vmcnt(1)
	ds_write_b128 v97, v[168:171]
	s_and_saveexec_b64 s[18:19], s[0:1]
	v_add3_u32 v97, s23, v216, v192
	ds_write_b128 v97, v[164:167]
	s_or_b64 exec, exec, s[18:19]
	s_cmpk_gt_u32 s17, 0x83
	s_cselect_b64 s[18:19], -1, 0
	v_lshl_add_u32 v97, s22, 14, v211
	s_and_b64 vcc, exec, s[18:19]
	s_waitcnt vmcnt(0)
	ds_write_b128 v97, v[172:175]
	s_cbranch_vccnz .LBB0_1886
	s_cmpk_lt_u32 s17, 0x7c
	s_cselect_b32 s22, 0, 0xffffffc0
	s_cselect_b32 s23, s74, s75
	s_add_i32 s22, s22, s76
	s_lshl_b32 s26, s22, 6
	s_add_i32 s26, s26, s23
	v_add_u32_e32 v97, s26, v189
	v_mad_i64_i32 v[98:99], s[22:23], v97, s62, v[196:197]
	global_load_dwordx4 v[168:171], v[98:99], off
	s_and_saveexec_b64 s[22:23], s[0:1]
	s_cbranch_execz .LBB0_1885
	v_add_u32_e32 v97, s26, v212
	v_mad_i64_i32 v[98:99], s[28:29], v97, s62, v[198:199]
	global_load_dwordx4 v[164:167], v[98:99], off
